# attention units mapped so the 8 workgroups of one (batch, head) run on the same XCD (K/V re-reads hit that XCD's L2)
# speedup vs baseline: 1.0004x; 1.0004x over previous
; template <int MODE>
; __device__ __forceinline__ void attn_unit(const bf16* __restrict__ qkv, bf16* __restrict__ O, const float* __restrict__ kmean, int b, int h, int qb, LAS unsigned char* ldsl, LAS unsigned char* lepi, int wid) {
;     const int lane = (int)__builtin_amdgcn_mbcnt_hi(~0u, __builtin_amdgcn_mbcnt_lo(~0u, 0u)), tid = wid * 64 + lane, r32 = lane & 31, hi = lane >> 5;
;     const size_t rowbase = (size_t)b * SEQ;
;     const bf16* Qp = qkv + (MODE == 0 ? 0 : 3 * 1024) + h * HD;
;     const bf16* Kp = Qp + 1024 + rowbase * PITCH; const bf16* Vp = Qp + 2048 + rowbase * PITCH;
;     LAS const unsigned char* K_lds = ldsl + 2 * SHM_V;
;     LAS float* ws = (LAS float*)(lepi + EPI_WS) + wid * 64; LAS float* li_l = ws; LAS float* al_l = ws + 32;
;     volatile LAS int* flags = (volatile LAS int*)(lepi + EPI_FLAG);
;     LAS unsigned char* q_lds = ldsl + LDS_Q + wid * 8192 + lane * 16;
;     const int qlo = qb * 256 + wid * 32, qpos = qlo + r32;
; #pragma unroll
;     for (int d0 = 0; d0 < 8; ++d0) *(LAS bf16x8*)(q_lds + d0 * 1024) = *(const bf16x8*)(Qp + (rowbase + qpos) * PITCH + d0 * 16 + hi * 8);
;     const int NT = 4 * (qb + 1);
;     const int vb0 = (int)(unsigned)(uintptr_t)ldsl + v_rd_base(lane);
;     unsigned koff0, koff1, voff0, voff1;
;     { const int b0 = tid * 16, b1 = b0 + 8192;
;       { const int row = b0 >> 8, cb = b0 & 255, colB = cb ^ ((row & 7) << 4); koff0 = (unsigned)(row * PITCH + (colB >> 1)) * 2u; }
;       { const int row = b1 >> 8, cb = b1 & 255, colB = cb ^ ((row & 7) << 4); koff1 = (unsigned)(row * PITCH + (colB >> 1)) * 2u; }
;       { const int st = b0 >> 9, wb = b0 & 511, kk = (st >> 2) * 8 + (wb >> 6), c = (st & 3) * 32 + ((wb & 63) >> 1), k = (kk & ~0xC) | ((kk & 4) << 1) | ((kk & 8) >> 1); voff0 = (unsigned)(k * PITCH + c) * 2u; }
;       { const int st = b1 >> 9, wb = b1 & 511, kk = (st >> 2) * 8 + (wb >> 6), c = (st & 3) * 32 + ((wb & 63) >> 1), k = (kk & ~0xC) | ((kk & 4) << 1) | ((kk & 8) >> 1); voff1 = (unsigned)(k * PITCH + c) * 2u; } }
;     const unsigned ldsw = (unsigned)wid * 1024u;
; __global__ void __launch_bounds__(NTHR, 2) fwd_kernel(Args args) {
;     ...
;         for (int p = wg; p < 256; p += G) { const int bh = p >> 3, k = p & 7, b = bh >> 3, h = bh & 7;
;             for (int s = 0; s < 2; ++s) att::attn_unit<1>(QKV, OB, kmean, b, h, s ? 15 - k : k, ring, lepi, wave_s); }
.LBB0_580:
	v_readlane_b32 s0, v254, 37
	v_readlane_b32 s1, v254, 38
	s_andn2_b64 vcc, exec, s[0:1]
	s_cbranch_vccnz .LBB0_942
	v_writelane_b32 v254, s72, 56
	v_writelane_b32 v254, s71, 57
	v_writelane_b32 v254, s70, 58
	v_writelane_b32 v254, s69, 59
	v_writelane_b32 v254, s68, 60
	v_writelane_b32 v254, s65, 61
	v_writelane_b32 v254, s96, 62
	v_writelane_b32 v254, s94, 63
	s_waitcnt vmcnt(0)
	v_lshlrev_b32_e32 v133, 4, v202
	v_lshlrev_b32_e32 v2, 3, v202
	v_writelane_b32 v255, s95, 0
	v_writelane_b32 v255, s90, 1
	s_lshl_b32 s0, s91, 2
	s_add_i32 s96, s0, 0
	s_lshl_b32 s0, s85, 13
	v_and_b32_e32 v3, 0xc0, v133
	v_lshlrev_b32_e32 v5, 1, v202
	s_add_i32 s0, s0, 0
	v_add_u32_e32 v0, s91, v202
	v_and_or_b32 v3, v2, 24, v3
	v_and_b32_e32 v5, 32, v5
	v_and_b32_e32 v2, 0x100, v2
	s_add_i32 s0, s0, 0x10000
	v_or3_b32 v5, v3, v5, v2
	v_lshlrev_b32_e32 v2, 4, v0
	v_add_u32_e32 v204, s0, v133
	v_add_u32_e32 v3, 0x2000, v2
	v_ashrrev_i32_e32 v6, 4, v0
	s_movk_i32 s0, 0x3000
	v_and_b32_e32 v2, 0xf0, v2
	v_and_b32_e32 v7, 0x70, v0
	v_mul_lo_u32 v8, v6, s0
	v_ashrrev_i32_e32 v3, 8, v3
	v_bitop3_b32 v134, v2, v8, v7 bitop3:0xde
	v_lshlrev_b32_e32 v7, 4, v3
	v_and_b32_e32 v7, 0x70, v7
	v_mul_i32_i24_e32 v8, 0x3000, v3
	v_bitop3_b32 v136, v7, v8, v2 bitop3:0xde
	v_bfe_u32 v7, v0, 2, 2
	v_and_b32_e32 v8, 0x60, v0
	v_lshlrev_b32_e32 v2, 3, v0
	v_lshrrev_b32_e32 v0, 1, v0
	v_and_b32_e32 v11, 8, v0
	v_lshrrev_b32_e32 v0, 1, v6
	v_and_b32_e32 v10, -16, v6
	v_and_b32_e32 v6, 4, v0
	v_writelane_b32 v255, s91, 2
	v_or_b32_e32 v0, v6, v10
	v_writelane_b32 v255, s85, 3
	v_and_b32_e32 v9, 24, v2
	v_or3_b32 v0, v0, v7, v11
	s_movk_i32 s3, 0x1800
	v_writelane_b32 v255, s66, 4
	s_load_dwordx2 s[4:5], s[66:67], 0xe0
	v_or_b32_e32 v2, v9, v8
	v_mul_lo_u32 v0, v0, s3
	v_or_b32_e32 v0, v0, v2
	v_lshlrev_b32_e32 v138, 1, v0
	v_lshrrev_b32_e32 v0, 1, v3
	v_and_b32_e32 v0, 4, v0
	s_mov_b32 s0, 0xfffff0
	s_add_i32 s96, s96, 0x20000
	v_and_or_b32 v0, v3, s0, v0
	v_writelane_b32 v255, s67, 5
	s_waitcnt lgkmcnt(0)
	s_add_u32 s1, s4, 0x41001800
	v_or3_b32 v0, v0, v7, v11
	v_writelane_b32 v255, s1, 6
	s_addc_u32 s1, s5, 0
	v_mul_i32_i24_e32 v12, 0x1800, v0
	v_writelane_b32 v255, s1, 8
	v_or_b32_e32 v0, v12, v2
	v_lshrrev_b32_e32 v4, 5, v202
	v_mov_b32_e32 v1, 0
	v_writelane_b32 v255, s91, 9
	v_lshlrev_b32_e32 v140, 1, v0
	v_and_b32_e32 v0, 0x60, v202
	v_writelane_b32 v255, s4, 10
	s_mov_b64 s[0:1], 0x290000
	v_lshlrev_b32_e32 v197, 4, v4
	v_lshl_add_u64 v[2:3], s[4:5], 0, v[0:1]
	s_movk_i32 s2, 0x70
	v_lshl_add_u64 v[142:143], v[2:3], 0, s[0:1]
	v_add_u32_e32 v2, 32, v197
	v_and_b32_e32 v3, 64, v202
	v_bitop3_b32 v208, v2, v133, s2 bitop3:0x78
	v_xor_b32_e32 v2, 1, v202
	v_add_u32_e32 v3, 64, v3
	v_lshlrev_b32_e32 v98, 14, v4
	v_mov_b32_e32 v99, v1
	s_mov_b64 s[0:1], 0x8000
	v_cmp_lt_i32_e32 vcc, v2, v3
	v_lshl_add_u64 v[106:107], v[98:99], 0, s[0:1]
	s_mov_b64 s[0:1], 0x9000
	v_cndmask_b32_e32 v2, v202, v2, vcc
	v_lshl_add_u64 v[108:109], v[98:99], 0, s[0:1]
	s_mov_b64 s[0:1], 0xa000
	v_lshlrev_b32_e32 v211, 2, v2
	v_and_b32_e32 v2, 1, v202
	v_lshl_add_u64 v[110:111], v[98:99], 0, s[0:1]
	s_mov_b64 s[0:1], 0xb000
	v_cmp_eq_u32_e64 s[8:9], 0, v2
	v_lshl_add_u64 v[112:113], v[98:99], 0, s[0:1]
	s_mov_b64 s[0:1], 0x18000
	v_or_b32_e32 v2, v10, v11
	v_lshl_add_u64 v[122:123], v[98:99], 0, s[0:1]
	s_mov_b64 s[0:1], 0x19000
	v_or3_b32 v2, v2, v6, v7
	v_lshl_add_u64 v[124:125], v[98:99], 0, s[0:1]
	s_mov_b64 s[0:1], 0x1a000
	v_mul_lo_u32 v2, v2, s3
	v_and_b32_e32 v0, 0x70, v133
	v_lshl_add_u64 v[126:127], v[98:99], 0, s[0:1]
	s_mov_b64 s[0:1], 0x1b000
	v_or3_b32 v2, v2, v8, v9
	v_and_b32_e32 v203, 31, v202
	v_bitop3_b32 v209, v197, v0, 64 bitop3:0x36
	v_add_u32_e32 v0, 0x60, v197
	v_lshl_add_u64 v[128:129], v[98:99], 0, s[0:1]
	v_lshlrev_b32_e32 v144, 1, v2
	v_or3_b32 v2, v12, v8, v9
	v_readlane_b32 s0, v254, 39
	v_writelane_b32 v255, s5, 11
	v_bitop3_b32 v210, v0, v133, s2 bitop3:0x78
	v_lshlrev_b32_e32 v0, 2, v4
	v_lshlrev_b32_e32 v146, 1, v2
	v_add_u32_e32 v2, s0, v203
	v_lshlrev_b32_e32 v132, 3, v4
	v_mov_b32_e32 v139, v1
	v_mov_b32_e32 v141, v1
	v_mov_b32_e32 v135, v1
	v_mov_b32_e32 v137, v1
	v_add_u32_e32 v205, 0, v5
	v_lshl_add_u32 v206, v203, 8, 0
	v_bitop3_b32 v207, v133, v197, s2 bitop3:0x6c
	v_cmp_gt_u32_e64 s[6:7], 32, v202
	v_lshl_add_u32 v198, v203, 2, s96
	v_or_b32_e32 v100, 0x1000, v98
	v_mov_b32_e32 v101, v1
	v_or_b32_e32 v102, 0x2000, v98
	v_mov_b32_e32 v103, v1
	v_or_b32_e32 v104, 0x3000, v98
	v_mov_b32_e32 v105, v1
	v_or_b32_e32 v114, 0x10000, v98
	v_mov_b32_e32 v115, v1
	v_or_b32_e32 v116, 0x11000, v98
	v_mov_b32_e32 v117, v1
	v_or_b32_e32 v118, 0x12000, v98
	v_mov_b32_e32 v119, v1
	v_or_b32_e32 v120, 0x13000, v98
	v_mov_b32_e32 v121, v1
	v_mov_b32_e32 v145, v1
	v_mov_b32_e32 v147, v1
	v_sub_u32_e32 v196, v2, v0
	s_mov_b64 s[2:3], 0x410c2800
	s_mov_b64 s[4:5], 0x410c2000
	s_mov_b32 s84, 0x41000000
	s_mov_b64 s[42:43], 0x41182800
	s_mov_b64 s[88:89], 0x41182000
	v_mov_b32_e32 v199, 0xff800000
	v_writelane_b32 v255, s93, 12
	v_readlane_b32 s93, v254, 32
	s_and_b32 s0, s93, 7
	s_lshl_b32 s0, s0, 5
	s_lshr_b32 s93, s93, 3
	s_or_b32 s93, s93, s0
	s_branch .LBB0_583

; template <int MODE>
; __device__ __forceinline__ void attn_unit(const bf16* __restrict__ qkv, bf16* __restrict__ O, const float* __restrict__ kmean, int b, int h, int qb, LAS unsigned char* ldsl, LAS unsigned char* lepi, int wid) {
;     const int lane = (int)__builtin_amdgcn_mbcnt_hi(~0u, __builtin_amdgcn_mbcnt_lo(~0u, 0u)), tid = wid * 64 + lane, r32 = lane & 31, hi = lane >> 5;
;     const size_t rowbase = (size_t)b * SEQ;
;     const bf16* Qp = qkv + (MODE == 0 ? 0 : 3 * 1024) + h * HD;
;     const bf16* Kp = Qp + 1024 + rowbase * PITCH; const bf16* Vp = Qp + 2048 + rowbase * PITCH;
;     LAS const unsigned char* K_lds = ldsl + 2 * SHM_V;
;     LAS float* ws = (LAS float*)(lepi + EPI_WS) + wid * 64; LAS float* li_l = ws; LAS float* al_l = ws + 32;
;     volatile LAS int* flags = (volatile LAS int*)(lepi + EPI_FLAG);
;     LAS unsigned char* q_lds = ldsl + LDS_Q + wid * 8192 + lane * 16;
;     const int qlo = qb * 256 + wid * 32, qpos = qlo + r32;
; #pragma unroll
;     for (int d0 = 0; d0 < 8; ++d0) *(LAS bf16x8*)(q_lds + d0 * 1024) = *(const bf16x8*)(Qp + (rowbase + qpos) * PITCH + d0 * 16 + hi * 8);
;     const int NT = 4 * (qb + 1);
;     const int vb0 = (int)(unsigned)(uintptr_t)ldsl + v_rd_base(lane);
;     unsigned koff0, koff1, voff0, voff1;
;     { const int b0 = tid * 16, b1 = b0 + 8192;
;       { const int row = b0 >> 8, cb = b0 & 255, colB = cb ^ ((row & 7) << 4); koff0 = (unsigned)(row * PITCH + (colB >> 1)) * 2u; }
;       { const int row = b1 >> 8, cb = b1 & 255, colB = cb ^ ((row & 7) << 4); koff1 = (unsigned)(row * PITCH + (colB >> 1)) * 2u; }
;       { const int st = b0 >> 9, wb = b0 & 511, kk = (st >> 2) * 8 + (wb >> 6), c = (st & 3) * 32 + ((wb & 63) >> 1), k = (kk & ~0xC) | ((kk & 4) << 1) | ((kk & 8) >> 1); voff0 = (unsigned)(k * PITCH + c) * 2u; }
;       { const int st = b1 >> 9, wb = b1 & 511, kk = (st >> 2) * 8 + (wb >> 6), c = (st & 3) * 32 + ((wb & 63) >> 1), k = (kk & ~0xC) | ((kk & 4) << 1) | ((kk & 8) >> 1); voff1 = (unsigned)(k * PITCH + c) * 2u; } }
;     const unsigned ldsw = (unsigned)wid * 1024u;
; __global__ void __launch_bounds__(NTHR, 2) fwd_kernel(Args args) {
;     ...
;         for (int p = wg; p < 256; p += G) { const int bh = p >> 3, k = p & 7, b = bh >> 3, h = bh & 7;
;             for (int s = 0; s < 2; ++s) att::attn_unit<0>(QKV, OB, kmean, b, h, s ? 15 - k : k, ring, lepi, wave_s); }
.LBB0_788:
	v_writelane_b32 v255, s80, 13
	v_and_b32_e32 v3, 0xf0, v133
	v_readlane_b32 s2, v255, 4
	v_readlane_b32 s3, v255, 5
	s_load_dwordx2 s[4:5], s[2:3], 0xe0
	v_readlane_b32 s1, v255, 3
	s_lshl_b32 s1, s1, 2
	v_readlane_b32 s2, v254, 40
	s_add_i32 s33, s1, 0
	s_add_i32 s33, s33, 0x20800
	v_add_u32_e32 v0, s2, v133
	s_waitcnt lgkmcnt(0)
	s_add_u32 s1, s4, 0x41000000
	v_ashrrev_i32_e32 v2, 8, v0
	v_writelane_b32 v255, s1, 14
	s_addc_u32 s1, s5, 0
	v_add_u32_e32 v1, 0x2000, v0
	v_lshlrev_b32_e32 v4, 4, v2
	v_writelane_b32 v255, s1, 15
	s_add_u32 s1, s4, 0x4d000000
	v_and_b32_e32 v4, 0x70, v4
	v_mul_i32_i24_e32 v5, 0x3000, v2
	v_ashrrev_i32_e32 v1, 8, v1
	v_writelane_b32 v255, s1, 16
	v_bitop3_b32 v132, v4, v5, v3 bitop3:0xde
	v_lshlrev_b32_e32 v4, 4, v1
	v_writelane_b32 v255, s4, 17
	v_and_b32_e32 v4, 0x70, v4
	v_mul_i32_i24_e32 v5, 0x3000, v1
	v_writelane_b32 v255, s5, 18
	s_addc_u32 s1, s5, 0
	v_bitop3_b32 v134, v4, v5, v3 bitop3:0xde
	v_lshrrev_b32_e32 v4, 1, v133
	v_writelane_b32 v255, s1, 19
	v_lshrrev_b32_e32 v0, 4, v0
	v_and_b32_e32 v4, 24, v4
	s_movk_i32 s1, 0x60
	v_lshrrev_b32_e32 v5, 1, v2
	v_and_or_b32 v0, v0, s1, v4
	v_lshrrev_b32_e32 v4, 5, v133
	v_and_b32_e32 v5, 4, v5
	s_mov_b32 s1, 0xfffff0
	v_bfe_u32 v3, v133, 6, 2
	v_and_b32_e32 v4, 8, v4
	v_and_or_b32 v2, v2, s1, v5
	v_or3_b32 v2, v2, v3, v4
	v_mul_i32_i24_e32 v2, 0x1800, v2
	v_or_b32_e32 v2, v2, v0
	v_lshlrev_b32_e32 v136, 1, v2
	v_lshrrev_b32_e32 v2, 1, v1
	v_readlane_b32 s2, v254, 63
	v_and_b32_e32 v2, 4, v2
	v_readlane_b32 s3, v255, 0
	v_and_or_b32 v1, v1, s1, v2
	s_load_dword s1, s[2:3], 0xf0
	v_or3_b32 v1, v1, v3, v4
	v_mul_i32_i24_e32 v1, 0x1800, v1
	v_or_b32_e32 v0, v1, v0
	v_mov_b32_e32 v1, 0
	s_waitcnt lgkmcnt(0)
	s_lshl_b32 s1, s1, 4
	v_readlane_b32 s12, v254, 32
	s_and_b32 s4, s12, 7
	s_lshl_b32 s4, s4, 5
	s_lshr_b32 s12, s12, 3
	s_or_b32 s12, s12, s4
	v_writelane_b32 v255, s1, 20
	s_add_i32 s1, 0, 0x20820
	v_lshlrev_b32_e32 v138, 1, v0
	v_mov_b32_e32 v137, v1
	v_mov_b32_e32 v139, v1
	v_mov_b32_e32 v133, v1
	v_mov_b32_e32 v135, v1
	v_cmp_eq_u32_e64 s[10:11], 0, v202
	v_add_u32_e32 v212, 0xffffff40, v196
	s_lshl_b32 s4, s12, 4
	v_mov_b32_e32 v131, v1
	s_mov_b64 s[42:43], 0x41181000
	s_mov_b64 s[88:89], 0x41180800
	s_mov_b32 s90, 0x3e0293ee
	s_mov_b32 s87, 0xc2400000
	s_add_i32 s91, 0, 0x20804
	s_add_i32 s86, 0, 0x20808
	s_add_i32 s2, 0, 0x2080c
	s_add_i32 s3, 0, 0x20810
	s_add_i32 s84, 0, 0x20814
	s_add_i32 s85, 0, 0x20818
	s_add_i32 s92, 0, 0x2081c
	v_writelane_b32 v255, s1, 10
	s_add_i32 s5, 0, 0x20824
	s_add_i32 s93, 0, 0x20828
	s_add_i32 s78, 0, 0x2082c
	s_add_i32 s79, 0, 0x20830
	s_add_i32 s94, 0, 0x20834
	s_add_i32 s95, 0, 0x20838
	s_add_i32 s96, 0, 0x2083c
	v_mov_b32_e32 v213, 0xff800000
	s_mov_b32 s14, s12
	s_branch .LBB0_790
